# v6 + pool prefix-sum loop with batched LDS reads
# baseline (speedup 1.0000x reference)
.LBB0_809:
	ds_read_u16 v120, v3
	ds_read_u16 v121, v3 offset:512
	ds_read_u16 v122, v3 offset:1024
	ds_read_u16 v123, v3 offset:1536
	v_add_u32_e32 v7, v3, v112
	ds_read_u16 v124, v7
	ds_read_u16 v125, v7 offset:512
	ds_read_u16 v126, v7 offset:1024
	ds_read_u16 v127, v7 offset:1536
	v_add_u32_e32 v6, s12, v2
	s_cmp_lg_u32 s12, 0
	s_cselect_b64 s[14:15], -1, 0
	v_cmp_ge_u32_e32 vcc, v6, v102
	v_add_u32_e32 v9, 1, v6
	v_min_u32_e32 v10, v9, v102
	v_cvt_f32_ubyte0_e32 v10, v10
	s_and_b64 s[16:17], s[14:15], vcc
	s_waitcnt lgkmcnt(0)
	v_lshlrev_b32_e32 v8, 16, v120
	v_add_f32_e32 v5, v5, v8
	v_lshlrev_b32_e32 v128, 16, v124
	v_cndmask_b32_e64 v128, 0, v128, s[16:17]
	v_sub_f32_e32 v5, v5, v128
	v_rcp_iflag_f32_e32 v10, v10
	v_cmp_ge_u32_e32 vcc, v9, v102
	v_fma_f32 v8, v10, v5, -v8
	v_bfe_u32 v10, v8, 16, 1
	v_add3_u32 v8, v8, v10, s11
	ds_write_b16_d16_hi v4, v8
	v_lshlrev_b32_e32 v8, 16, v121
	v_add_f32_e32 v5, v5, v8
	v_lshlrev_b32_e32 v128, 16, v125
	v_cndmask_b32_e32 v128, 0, v128, vcc
	v_sub_f32_e32 v5, v5, v128
	v_add_u32_e32 v9, 2, v6
	v_min_u32_e32 v10, v9, v102
	v_cvt_f32_ubyte0_e32 v10, v10
	v_rcp_iflag_f32_e32 v10, v10
	v_cmp_ge_u32_e32 vcc, v9, v102
	v_fma_f32 v8, v10, v5, -v8
	v_bfe_u32 v10, v8, 16, 1
	v_add3_u32 v8, v8, v10, s11
	ds_write_b16_d16_hi v4, v8 offset:528
	v_lshlrev_b32_e32 v8, 16, v122
	v_add_f32_e32 v5, v5, v8
	v_lshlrev_b32_e32 v128, 16, v126
	v_cndmask_b32_e32 v128, 0, v128, vcc
	v_sub_f32_e32 v5, v5, v128
	v_add_u32_e32 v9, 3, v6
	v_min_u32_e32 v10, v9, v102
	v_cvt_f32_ubyte0_e32 v10, v10
	v_rcp_iflag_f32_e32 v10, v10
	v_cmp_ge_u32_e32 vcc, v9, v102
	v_fma_f32 v8, v10, v5, -v8
	v_bfe_u32 v10, v8, 16, 1
	v_add3_u32 v8, v8, v10, s11
	ds_write_b16_d16_hi v4, v8 offset:1056
	v_lshlrev_b32_e32 v8, 16, v123
	v_add_f32_e32 v5, v5, v8
	v_lshlrev_b32_e32 v128, 16, v127
	v_cndmask_b32_e32 v128, 0, v128, vcc
	v_sub_f32_e32 v5, v5, v128
	v_add_u32_e32 v6, 4, v6
	v_min_u32_e32 v6, v6, v102
	v_cvt_f32_ubyte0_e32 v6, v6
	v_rcp_iflag_f32_e32 v6, v6
	s_add_i32 s12, s12, 4
	s_cmp_eq_u32 s12, 32
	v_add_u32_e32 v3, 0x800, v3
	v_fma_f32 v6, v6, v5, -v8
	v_bfe_u32 v7, v6, 16, 1
	v_add3_u32 v6, v6, v7, s11
	ds_write_b16_d16_hi v4, v6 offset:1584
	v_add_u32_e32 v4, 0x840, v4
	s_cbranch_scc1 .LBB0_782
	s_branch .LBB0_809
